# P1 stage S5: row loads of token blocks 1..3 issued ahead of the group's vector loads (no per-block load->drain chain)
# baseline (speedup 1.0000x reference)
.LBB0_594:
	v_add_u32_e32 v138, s8, v175
	v_ashrrev_i32_e32 v139, 31, v138
	v_lshlrev_b64 v[110:111], 2, v[138:139]
	v_lshl_add_u64 v[112:113], s[4:5], 0, v[110:111]
	v_lshl_add_u64 v[140:141], v[138:139], 1, s[6:7]
	s_and_b64 vcc, exec, s[0:1]
	s_cbranch_vccnz .Lp1s5_a
	v_lshl_add_u64 v[30:31], v[140:141], 0, v[180:181]
	global_load_dwordx4 v[18:21], v[30:31], off
	v_lshl_add_u64 v[30:31], v[140:141], 0, v[182:183]
	global_load_dwordx4 v[22:25], v[30:31], off
	v_lshl_add_u64 v[30:31], v[140:141], 0, v[184:185]
	global_load_dwordx4 v[26:29], v[30:31], off
.Lp1s5_a:
	global_load_dwordx4 v[142:145], v[112:113], off
	global_load_dwordx4 v[146:149], v[112:113], off offset:16
	v_lshl_add_u64 v[112:113], v[140:141], 0, v[178:179]
	global_load_dwordx4 v[150:153], v[112:113], off
	v_lshl_add_u64 v[112:113], s[50:51], 0, v[110:111]
	global_load_dwordx4 v[154:157], v[112:113], off
	global_load_dwordx4 v[158:161], v[112:113], off offset:16
	v_lshl_add_u64 v[110:111], s[10:11], 0, v[110:111]
	global_load_dwordx4 v[114:117], v[110:111], off
	s_nop 0
	global_load_dwordx4 v[110:113], v[110:111], off offset:16
	v_mov_b32_e32 v162, 0
	v_mov_b32_e32 v163, 0
	s_and_b64 vcc, exec, s[0:1]
	s_waitcnt vmcnt(6)
	v_pk_add_f32 v[144:145], v[144:145], 1.0 op_sel_hi:[1,0]
	v_pk_add_f32 v[164:165], v[142:143], 1.0 op_sel_hi:[1,0]
	s_waitcnt vmcnt(5)
	v_pk_add_f32 v[148:149], v[148:149], 1.0 op_sel_hi:[1,0]
	v_pk_add_f32 v[166:167], v[146:147], 1.0 op_sel_hi:[1,0]
	s_waitcnt vmcnt(4)
	v_lshlrev_b32_e32 v168, 16, v150
	v_and_b32_e32 v169, 0xffff0000, v150
	v_lshlrev_b32_e32 v176, 16, v152
	v_and_b32_e32 v177, 0xffff0000, v152
	s_waitcnt vmcnt(3)
	v_pk_mul_f32 v[142:143], v[156:157], v[144:145]
	v_pk_mul_f32 v[146:147], v[154:155], v[164:165]
	s_waitcnt vmcnt(2)
	v_pk_mul_f32 v[144:145], v[160:161], v[148:149]
	v_pk_mul_f32 v[148:149], v[158:159], v[166:167]
	v_pk_mul_f32 v[154:155], v[120:121], v[168:169]
	v_pk_mul_f32 v[156:157], v[120:121], v[176:177]
	s_waitcnt vmcnt(1)
	v_pk_fma_f32 v[154:155], v[146:147], v[154:155], v[114:115]
	s_waitcnt vmcnt(0)
	v_pk_fma_f32 v[156:157], v[148:149], v[156:157], v[110:111]
	v_cvt_pk_fp8_f32 v162, v154, v155
	v_cvt_pk_fp8_f32 v163, v156, v157
	v_lshlrev_b32_e32 v150, 16, v151
	v_and_b32_e32 v151, 0xffff0000, v151
	v_lshlrev_b32_e32 v152, 16, v153
	v_and_b32_e32 v153, 0xffff0000, v153
	v_pk_mul_f32 v[150:151], v[124:125], v[150:151]
	v_pk_mul_f32 v[152:153], v[124:125], v[152:153]
	v_pk_fma_f32 v[150:151], v[142:143], v[150:151], v[116:117]
	v_pk_fma_f32 v[152:153], v[144:145], v[152:153], v[112:113]
	v_cvt_pk_fp8_f32 v162, v150, v151 op_sel:[0,0,1]
	v_cvt_pk_fp8_f32 v163, v152, v153 op_sel:[0,0,1]
	v_lshl_add_u64 v[150:151], s[38:39], 0, v[138:139]
	v_lshl_add_u64 v[152:153], v[150:151], 0, v[16:17]
	global_store_dwordx2 v[152:153], v[162:163], off
	s_cbranch_vccnz .LBB0_596
	v_mov_b32_e32 v152, v18
	v_mov_b32_e32 v153, v19
	v_mov_b32_e32 v154, v20
	v_mov_b32_e32 v155, v21
	v_mov_b32_e32 v156, v8
	v_mov_b32_e32 v157, v8
	v_lshlrev_b32_e32 v158, 16, v152
	v_and_b32_e32 v159, 0xffff0000, v152
	v_lshlrev_b32_e32 v160, 16, v154
	v_and_b32_e32 v161, 0xffff0000, v154
	v_pk_mul_f32 v[158:159], v[118:119], v[158:159]
	v_pk_mul_f32 v[160:161], v[118:119], v[160:161]
	v_pk_fma_f32 v[158:159], v[146:147], v[158:159], v[114:115]
	v_pk_fma_f32 v[160:161], v[148:149], v[160:161], v[110:111]
	v_cvt_pk_fp8_f32 v156, v158, v159
	v_cvt_pk_fp8_f32 v157, v160, v161
	v_lshlrev_b32_e32 v152, 16, v153
	v_and_b32_e32 v153, 0xffff0000, v153
	v_lshlrev_b32_e32 v154, 16, v155
	v_and_b32_e32 v155, 0xffff0000, v155
	v_pk_mul_f32 v[152:153], v[126:127], v[152:153]
	v_pk_mul_f32 v[154:155], v[126:127], v[154:155]
	v_pk_fma_f32 v[152:153], v[142:143], v[152:153], v[116:117]
	v_pk_fma_f32 v[154:155], v[144:145], v[154:155], v[112:113]
	v_cvt_pk_fp8_f32 v156, v152, v153 op_sel:[0,0,1]
	v_cvt_pk_fp8_f32 v157, v154, v155 op_sel:[0,0,1]
	v_lshl_add_u64 v[152:153], v[150:151], 0, v[128:129]
	global_store_dwordx2 v[152:153], v[156:157], off
	v_mov_b32_e32 v152, v22
	v_mov_b32_e32 v153, v23
	v_mov_b32_e32 v154, v24
	v_mov_b32_e32 v155, v25
	v_mov_b32_e32 v156, v8
	v_mov_b32_e32 v157, v8
	v_lshlrev_b32_e32 v158, 16, v152
	v_and_b32_e32 v159, 0xffff0000, v152
	v_lshlrev_b32_e32 v160, 16, v154
	v_and_b32_e32 v161, 0xffff0000, v154
	v_pk_mul_f32 v[158:159], v[10:11], v[158:159]
	v_pk_mul_f32 v[160:161], v[10:11], v[160:161]
	v_pk_fma_f32 v[158:159], v[146:147], v[158:159], v[114:115]
	v_pk_fma_f32 v[160:161], v[148:149], v[160:161], v[110:111]
	v_cvt_pk_fp8_f32 v156, v158, v159
	v_cvt_pk_fp8_f32 v157, v160, v161
	v_lshlrev_b32_e32 v152, 16, v153
	v_and_b32_e32 v153, 0xffff0000, v153
	v_lshlrev_b32_e32 v154, 16, v155
	v_and_b32_e32 v155, 0xffff0000, v155
	v_pk_mul_f32 v[152:153], v[130:131], v[152:153]
	v_pk_mul_f32 v[154:155], v[130:131], v[154:155]
	v_pk_fma_f32 v[152:153], v[142:143], v[152:153], v[116:117]
	v_pk_fma_f32 v[154:155], v[144:145], v[154:155], v[112:113]
	v_cvt_pk_fp8_f32 v156, v152, v153 op_sel:[0,0,1]
	v_cvt_pk_fp8_f32 v157, v154, v155 op_sel:[0,0,1]
	v_lshl_add_u64 v[152:153], v[150:151], 0, v[132:133]
	global_store_dwordx2 v[152:153], v[156:157], off
	v_mov_b32_e32 v152, v26
	v_mov_b32_e32 v153, v27
	v_mov_b32_e32 v154, v28
	v_mov_b32_e32 v155, v29
	v_mov_b32_e32 v140, v8
	v_mov_b32_e32 v141, v8
	v_lshlrev_b32_e32 v156, 16, v152
	v_and_b32_e32 v157, 0xffff0000, v152
	v_lshlrev_b32_e32 v158, 16, v154
	v_and_b32_e32 v159, 0xffff0000, v154
	v_pk_mul_f32 v[156:157], v[122:123], v[156:157]
	v_pk_mul_f32 v[158:159], v[122:123], v[158:159]
	v_pk_fma_f32 v[114:115], v[146:147], v[156:157], v[114:115]
	v_pk_fma_f32 v[110:111], v[148:149], v[158:159], v[110:111]
	v_cvt_pk_fp8_f32 v140, v114, v115
	v_cvt_pk_fp8_f32 v141, v110, v111
	v_lshlrev_b32_e32 v152, 16, v153
	v_and_b32_e32 v153, 0xffff0000, v153
	v_lshlrev_b32_e32 v154, 16, v155
	v_and_b32_e32 v155, 0xffff0000, v155
	v_pk_mul_f32 v[152:153], v[134:135], v[152:153]
	v_pk_mul_f32 v[154:155], v[134:135], v[154:155]
	v_pk_fma_f32 v[110:111], v[142:143], v[152:153], v[116:117]
	v_pk_fma_f32 v[112:113], v[144:145], v[154:155], v[112:113]
	v_cvt_pk_fp8_f32 v140, v110, v111 op_sel:[0,0,1]
	v_cvt_pk_fp8_f32 v141, v112, v113 op_sel:[0,0,1]
	v_lshl_add_u64 v[110:111], v[150:151], 0, v[136:137]
	global_store_dwordx2 v[110:111], v[140:141], off
.LBB0_596:
	v_add_u32_e32 v160, 32, v138
	v_ashrrev_i32_e32 v161, 31, v160
	v_lshlrev_b64 v[110:111], 2, v[160:161]
	v_lshl_add_u64 v[112:113], s[4:5], 0, v[110:111]
	v_lshl_add_u64 v[138:139], v[160:161], 1, s[6:7]
	s_and_b64 vcc, exec, s[0:1]
	s_cbranch_vccnz .Lp1s5_b
	v_lshl_add_u64 v[30:31], v[138:139], 0, v[180:181]
	global_load_dwordx4 v[18:21], v[30:31], off
	v_lshl_add_u64 v[30:31], v[138:139], 0, v[182:183]
	global_load_dwordx4 v[22:25], v[30:31], off
	v_lshl_add_u64 v[30:31], v[138:139], 0, v[184:185]
	global_load_dwordx4 v[26:29], v[30:31], off
.Lp1s5_b:
	global_load_dwordx4 v[140:143], v[112:113], off
	global_load_dwordx4 v[144:147], v[112:113], off offset:16
	v_lshl_add_u64 v[112:113], v[138:139], 0, v[178:179]
	global_load_dwordx4 v[148:151], v[112:113], off
	v_lshl_add_u64 v[112:113], s[50:51], 0, v[110:111]
	global_load_dwordx4 v[152:155], v[112:113], off
	global_load_dwordx4 v[156:159], v[112:113], off offset:16
	v_lshl_add_u64 v[110:111], s[10:11], 0, v[110:111]
	global_load_dwordx4 v[114:117], v[110:111], off
	s_nop 0
	global_load_dwordx4 v[110:113], v[110:111], off offset:16
	v_mov_b32_e32 v162, 0
	v_mov_b32_e32 v163, 0
	s_and_b64 vcc, exec, s[0:1]
	s_waitcnt vmcnt(6)
	v_pk_add_f32 v[142:143], v[142:143], 1.0 op_sel_hi:[1,0]
	v_pk_add_f32 v[164:165], v[140:141], 1.0 op_sel_hi:[1,0]
	s_waitcnt vmcnt(5)
	v_pk_add_f32 v[146:147], v[146:147], 1.0 op_sel_hi:[1,0]
	v_pk_add_f32 v[166:167], v[144:145], 1.0 op_sel_hi:[1,0]
	s_waitcnt vmcnt(4)
	v_lshlrev_b32_e32 v168, 16, v148
	v_and_b32_e32 v169, 0xffff0000, v148
	v_lshlrev_b32_e32 v176, 16, v150
	v_and_b32_e32 v177, 0xffff0000, v150
	s_waitcnt vmcnt(3)
	v_pk_mul_f32 v[140:141], v[154:155], v[142:143]
	v_pk_mul_f32 v[144:145], v[152:153], v[164:165]
	s_waitcnt vmcnt(2)
	v_pk_mul_f32 v[142:143], v[158:159], v[146:147]
	v_pk_mul_f32 v[146:147], v[156:157], v[166:167]
	v_pk_mul_f32 v[152:153], v[120:121], v[168:169]
	v_pk_mul_f32 v[154:155], v[120:121], v[176:177]
	s_waitcnt vmcnt(1)
	v_pk_fma_f32 v[152:153], v[144:145], v[152:153], v[114:115]
	s_waitcnt vmcnt(0)
	v_pk_fma_f32 v[154:155], v[146:147], v[154:155], v[110:111]
	v_cvt_pk_fp8_f32 v162, v152, v153
	v_cvt_pk_fp8_f32 v163, v154, v155
	v_lshlrev_b32_e32 v148, 16, v149
	v_and_b32_e32 v149, 0xffff0000, v149
	v_lshlrev_b32_e32 v150, 16, v151
	v_and_b32_e32 v151, 0xffff0000, v151
	v_pk_mul_f32 v[148:149], v[124:125], v[148:149]
	v_pk_mul_f32 v[150:151], v[124:125], v[150:151]
	v_pk_fma_f32 v[148:149], v[140:141], v[148:149], v[116:117]
	v_pk_fma_f32 v[150:151], v[142:143], v[150:151], v[112:113]
	v_cvt_pk_fp8_f32 v162, v148, v149 op_sel:[0,0,1]
	v_cvt_pk_fp8_f32 v163, v150, v151 op_sel:[0,0,1]
	v_lshl_add_u64 v[148:149], s[38:39], 0, v[160:161]
	v_lshl_add_u64 v[150:151], v[148:149], 0, v[16:17]
	global_store_dwordx2 v[150:151], v[162:163], off
	s_cbranch_vccnz .LBB0_593
	v_mov_b32_e32 v150, v18
	v_mov_b32_e32 v151, v19
	v_mov_b32_e32 v152, v20
	v_mov_b32_e32 v153, v21
	v_mov_b32_e32 v154, v8
	v_mov_b32_e32 v155, v8
	v_lshlrev_b32_e32 v156, 16, v150
	v_and_b32_e32 v157, 0xffff0000, v150
	v_lshlrev_b32_e32 v158, 16, v152
	v_and_b32_e32 v159, 0xffff0000, v152
	v_pk_mul_f32 v[156:157], v[118:119], v[156:157]
	v_pk_mul_f32 v[158:159], v[118:119], v[158:159]
	v_pk_fma_f32 v[156:157], v[144:145], v[156:157], v[114:115]
	v_pk_fma_f32 v[158:159], v[146:147], v[158:159], v[110:111]
	v_cvt_pk_fp8_f32 v154, v156, v157
	v_cvt_pk_fp8_f32 v155, v158, v159
	v_lshlrev_b32_e32 v150, 16, v151
	v_and_b32_e32 v151, 0xffff0000, v151
	v_lshlrev_b32_e32 v152, 16, v153
	v_and_b32_e32 v153, 0xffff0000, v153
	v_pk_mul_f32 v[150:151], v[126:127], v[150:151]
	v_pk_mul_f32 v[152:153], v[126:127], v[152:153]
	v_pk_fma_f32 v[150:151], v[140:141], v[150:151], v[116:117]
	v_pk_fma_f32 v[152:153], v[142:143], v[152:153], v[112:113]
	v_cvt_pk_fp8_f32 v154, v150, v151 op_sel:[0,0,1]
	v_cvt_pk_fp8_f32 v155, v152, v153 op_sel:[0,0,1]
	v_lshl_add_u64 v[150:151], v[148:149], 0, v[128:129]
	global_store_dwordx2 v[150:151], v[154:155], off
	v_mov_b32_e32 v150, v22
	v_mov_b32_e32 v151, v23
	v_mov_b32_e32 v152, v24
	v_mov_b32_e32 v153, v25
	v_mov_b32_e32 v154, v8
	v_mov_b32_e32 v155, v8
	v_lshlrev_b32_e32 v156, 16, v150
	v_and_b32_e32 v157, 0xffff0000, v150
	v_lshlrev_b32_e32 v158, 16, v152
	v_and_b32_e32 v159, 0xffff0000, v152
	v_pk_mul_f32 v[156:157], v[10:11], v[156:157]
	v_pk_mul_f32 v[158:159], v[10:11], v[158:159]
	v_pk_fma_f32 v[156:157], v[144:145], v[156:157], v[114:115]
	v_pk_fma_f32 v[158:159], v[146:147], v[158:159], v[110:111]
	v_cvt_pk_fp8_f32 v154, v156, v157
	v_cvt_pk_fp8_f32 v155, v158, v159
	v_lshlrev_b32_e32 v150, 16, v151
	v_and_b32_e32 v151, 0xffff0000, v151
	v_lshlrev_b32_e32 v152, 16, v153
	v_and_b32_e32 v153, 0xffff0000, v153
	v_pk_mul_f32 v[150:151], v[130:131], v[150:151]
	v_pk_mul_f32 v[152:153], v[130:131], v[152:153]
	v_pk_fma_f32 v[150:151], v[140:141], v[150:151], v[116:117]
	v_pk_fma_f32 v[152:153], v[142:143], v[152:153], v[112:113]
	v_cvt_pk_fp8_f32 v154, v150, v151 op_sel:[0,0,1]
	v_cvt_pk_fp8_f32 v155, v152, v153 op_sel:[0,0,1]
	v_lshl_add_u64 v[150:151], v[148:149], 0, v[132:133]
	global_store_dwordx2 v[150:151], v[154:155], off
	v_mov_b32_e32 v150, v26
	v_mov_b32_e32 v151, v27
	v_mov_b32_e32 v152, v28
	v_mov_b32_e32 v153, v29
	v_mov_b32_e32 v138, v8
	v_mov_b32_e32 v139, v8
	v_lshlrev_b32_e32 v154, 16, v150
	v_and_b32_e32 v155, 0xffff0000, v150
	v_lshlrev_b32_e32 v156, 16, v152
	v_and_b32_e32 v157, 0xffff0000, v152
	v_pk_mul_f32 v[154:155], v[122:123], v[154:155]
	v_pk_mul_f32 v[156:157], v[122:123], v[156:157]
	v_pk_fma_f32 v[114:115], v[144:145], v[154:155], v[114:115]
	v_pk_fma_f32 v[110:111], v[146:147], v[156:157], v[110:111]
	v_cvt_pk_fp8_f32 v138, v114, v115
	v_cvt_pk_fp8_f32 v139, v110, v111
	v_lshlrev_b32_e32 v150, 16, v151
	v_and_b32_e32 v151, 0xffff0000, v151
	v_lshlrev_b32_e32 v152, 16, v153
	v_and_b32_e32 v153, 0xffff0000, v153
	v_pk_mul_f32 v[150:151], v[134:135], v[150:151]
	v_pk_mul_f32 v[152:153], v[134:135], v[152:153]
	v_pk_fma_f32 v[110:111], v[140:141], v[150:151], v[116:117]
	v_pk_fma_f32 v[112:113], v[142:143], v[152:153], v[112:113]
	v_cvt_pk_fp8_f32 v138, v110, v111 op_sel:[0,0,1]
	v_cvt_pk_fp8_f32 v139, v112, v113 op_sel:[0,0,1]
	v_lshl_add_u64 v[110:111], v[148:149], 0, v[136:137]
	global_store_dwordx2 v[110:111], v[138:139], off
	s_branch .LBB0_593
